# adds: next unit row-statistics loads hoisted to the epilogue start in in-proj, uq, ukv GEMM phases
# baseline (speedup 1.0000x reference)
; #define LAS __attribute__((address_space(3)))
; __device__ __forceinline__ float rstd_part8(const float* p, float inv_n) { const f32x4 a = ((const f32x4*)p)[0], b = ((const f32x4*)p)[1]; const f32x4 s4 = a + b; return 1.0f / sqrtf(((s4[0] + s4[1]) + (s4[2] + s4[3])) * inv_n + EPS); }
;     EPI_NOMID
;     __device__ __forceinline__ void begin(const Unit& u, int ui, int tid, LAS unsigned char* lds) const { if (tid < 256) rtab_put(lds, ui, tid, rstd_part8(RS + (size_t)(u.pm * 256 + tid) * 8, 1.f / QRANK) * QS_MLA, 0.f); }
.LBB0_656:
	s_and_b64 vcc, exec, s[10:11]
	s_cbranch_vccnz .Lpf_uq_skip
	s_and_saveexec_b64 s[100:101], s[8:9]
	v_lshl_add_u32 v244, s62, 8, v188
	v_ashrrev_i32_e32 v245, 31, v244
	v_lshlrev_b64 v[244:245], 5, v[244:245]
	v_lshl_add_u64 v[244:245], s[16:17], 0, v[244:245]
	global_load_dwordx4 v[240:243], v[244:245], off
	global_load_dwordx4 v[228:231], v[244:245], off offset:16
	s_mov_b64 exec, s[100:101]

; #define LAS __attribute__((address_space(3)))
; __device__ __forceinline__ float rstd_part8(const float* p, float inv_n) { const f32x4 a = ((const f32x4*)p)[0], b = ((const f32x4*)p)[1]; const f32x4 s4 = a + b; return 1.0f / sqrtf(((s4[0] + s4[1]) + (s4[2] + s4[3])) * inv_n + EPS); }
;     EPI_NOMID
;     __device__ __forceinline__ void begin(const Unit& u, int ui, int tid, LAS unsigned char* lds) const { if (tid < 256) rtab_put(lds, ui, tid, rstd_part8(RS + (size_t)(u.pm * 256 + tid) * 8, 1.f / QRANK) * QS_MLA, 0.f); }
.LBB0_688:
	v_cvt_pk_bf16_f32 v2, v6, v7
	v_cvt_pk_bf16_f32 v3, v8, v9
	v_cvt_pk_bf16_f32 v4, v18, v19
	v_cvt_pk_bf16_f32 v5, v12, v13
	flat_store_dwordx4 v[10:11], v[2:5] offset:256
	s_mov_b64 s[12:13], -1
	s_and_b64 vcc, exec, s[10:11]
	v_readfirstlane_b32 s3, v0
	s_cbranch_vccnz .LBB0_649
	s_and_saveexec_b64 s[12:13], s[8:9]
	s_cbranch_execz .LBB0_691
	s_mov_b32 s3, 0xf800000
	s_waitcnt vmcnt(0) lgkmcnt(0)
	v_mov_b32_e32 v2, v240
	v_mov_b32_e32 v3, v241
	v_mov_b32_e32 v4, v242
	v_mov_b32_e32 v5, v243
	v_mov_b32_e32 v6, v228
	v_mov_b32_e32 v7, v229
	v_mov_b32_e32 v8, v230
	v_mov_b32_e32 v9, v231
	v_pk_add_f32 v[4:5], v[4:5], v[8:9]
	v_pk_add_f32 v[2:3], v[2:3], v[6:7]
	s_nop 0
	v_pk_mov_b32 v[6:7], v[2:3], v[4:5] op_sel:[1,0]
	v_mov_b32_e32 v3, v5
	v_pk_add_f32 v[2:3], v[6:7], v[2:3]
	s_nop 0
	v_add_f32_e32 v0, v2, v3
	v_fmamk_f32 v0, v0, 0x3b2aaaab, v236
	v_cmp_gt_f32_e32 vcc, s3, v0
	v_mul_f32_e32 v2, 0x4f800000, v0
	s_add_i32 s3, s60, 0x100
	v_cndmask_b32_e32 v0, v0, v2, vcc
	v_sqrt_f32_e32 v2, v0
	s_and_b32 s3, s3, 0x100
	s_lshl_b32 s3, s3, 3
	s_add_i32 s3, s3, 0
	v_add_u32_e32 v3, -1, v2
	v_fma_f32 v4, -v3, v2, v0
	v_cmp_ge_f32_e64 s[10:11], 0, v4
	v_add_u32_e32 v4, 1, v2
	s_nop 0
	v_cndmask_b32_e64 v3, v2, v3, s[10:11]
	v_fma_f32 v2, -v4, v2, v0
	v_cmp_lt_f32_e64 s[10:11], 0, v2
	s_nop 1
	v_cndmask_b32_e64 v2, v3, v4, s[10:11]
	v_mul_f32_e32 v3, 0x37800000, v2
	v_cndmask_b32_e32 v2, v2, v3, vcc
	v_cmp_class_f32_e32 vcc, v0, v251
	s_nop 1
	v_cndmask_b32_e32 v0, v2, v0, vcc
	v_div_scale_f32 v2, s[6:7], v0, v0, 1.0
	v_rcp_f32_e32 v3, v2
	s_nop 0
	v_fma_f32 v4, -v2, v3, 1.0
	v_fmac_f32_e32 v3, v4, v3
	v_div_scale_f32 v4, vcc, 1.0, v0, 1.0
	v_mul_f32_e32 v5, v4, v3
	v_fma_f32 v6, -v2, v5, v4
	v_fmac_f32_e32 v5, v6, v3
	v_fma_f32 v2, -v2, v5, v4
	v_div_fmas_f32 v2, v2, v3, v5
	v_div_fixup_f32 v0, v2, v0, 1.0
	v_mov_b32_e32 v2, v188
	v_mul_f32_e32 v0, 0x3e16c740, v0
	v_lshl_add_u32 v2, v2, 3, s3
	v_add_u32_e32 v2, 0x22400, v2
	ds_write_b64 v2, v[0:1]

; #define LAS __attribute__((address_space(3)))
; __device__ __forceinline__ u32x4 pack8(f32x4 a, f32x4 b) { u32x4 w; w.x = pk2(a[0], a[1]); w.y = pk2(a[2], a[3]); w.z = pk2(b[0], b[1]); w.w = pk2(b[2], b[3]); return w; }
; __device__ __forceinline__ float rstd_part4(const float* p, float inv_n) { const f32x4 a = ((const f32x4*)p)[0]; return 1.0f / sqrtf(((a[0] + a[1]) + (a[2] + a[3])) * inv_n + EPS); }
; __device__ __forceinline__ f32x2 rtab_get(LAS unsigned char* lds, int ui, int r) { return ((const LAS f32x2*)(lds + RTAB_OFF))[(ui & 1) * 256 + r]; }
;     EPI_NOMID
;     __device__ __forceinline__ void begin(const Unit& u, int ui, int tid, LAS unsigned char* lds) const { if (tid < 256) rtab_put(lds, ui, tid, rstd_part4(RS + (size_t)(u.pm * 256 + tid) * 4, 1.f / KVRANK), 0.f); }
;     __device__ __forceinline__ void operator()(const f32x4 (&acc)[2][2][4][2], const Unit& u, int ui, int wr, int wc, int fr, int fq, LAS unsigned char* lds) const {
;         bf16_t* dst = u.pn < 2 ? KN : VM; const int cb = (u.pn & 1) * 256;
; #pragma unroll
;         for (int ai = 0; ai < 2; ++ai)
; #pragma unroll
;             for (int m = 0; m < 4; ++m) {
;                 const int rr = ai * 128 + wr * 64 + m * 16 + fr, row = u.pm * 256 + rr; const float rs = rtab_get(lds, ui, rr)[0];
; #pragma unroll
;                 for (int bj = 0; bj < 2; ++bj) { const int c = cb + bj * 128 + wc * 32 + fq * 8;
;                     *(u32x4*)(dst + (size_t)row * 512 + c) = pack8(acc[ai][bj][m][0] * rs, acc[ai][bj][m][1] * rs); }
.LBB0_713:
	s_and_b64 vcc, exec, s[10:11]
	s_cbranch_vccnz .Lpf_ukv_skip
	s_and_saveexec_b64 s[100:101], s[8:9]
	v_lshl_add_u32 v244, s45, 8, v188
	v_ashrrev_i32_e32 v245, 31, v244
	v_lshl_add_u64 v[244:245], v[244:245], 4, s[14:15]
	global_load_dwordx4 v[240:243], v[244:245], off
	s_mov_b64 exec, s[100:101]
.Lpf_ukv_skip:
	s_cmp_lt_i32 s47, 2
	s_mov_b32 s35, 0x1e800000
	s_cselect_b32 s35, s35, 0x20800000
	s_add_u32 s36, s74, s35
	s_addc_u32 s37, s75, 0
	s_lshl_b32 s35, s47, 8
	s_and_b32 s47, s44, 0x100
	v_mov_b32_e32 v0, v188
	s_lshl_b32 s47, s47, 3
	s_add_i32 s47, s47, 0
	v_and_or_b32 v134, v0, 15, s40
	v_lshl_add_u32 v135, v134, 3, s47
	v_add_u32_e32 v139, 0x22400, v135
	ds_read_b32 v140, v139
	s_and_b32 s35, s35, 0x100
	v_lshrrev_b32_e32 v0, 1, v0
	v_lshl_add_u32 v134, s46, 8, v134
	v_and_or_b32 v0, v0, 24, s35
	v_ashrrev_i32_e32 v135, 31, v134
	v_or_b32_e32 v0, s41, v0
	v_lshlrev_b64 v[142:143], 10, v[134:135]
	v_lshl_add_u64 v[142:143], s[36:37], 0, v[142:143]
	s_waitcnt lgkmcnt(0)
	v_pk_mul_f32 v[128:129], v[128:129], v[140:141] op_sel_hi:[1,0]
	v_pk_mul_f32 v[126:127], v[126:127], v[140:141] op_sel_hi:[1,0]
	v_pk_mul_f32 v[144:145], v[124:125], v[140:141] op_sel_hi:[1,0]
	v_pk_mul_f32 v[124:125], v[122:123], v[140:141] op_sel_hi:[1,0]
	v_lshlrev_b32_e32 v0, 1, v0
	v_cvt_pk_bf16_f32 v122, v126, v127
	v_cvt_pk_bf16_f32 v123, v128, v129
	v_cvt_pk_bf16_f32 v124, v124, v125
	v_cvt_pk_bf16_f32 v125, v144, v145
	v_lshl_add_u64 v[126:127], v[142:143], 0, v[0:1]
	flat_store_dwordx4 v[126:127], v[122:125]
	v_pk_mul_f32 v[120:121], v[120:121], v[140:141] op_sel_hi:[1,0]
	v_pk_mul_f32 v[118:119], v[118:119], v[140:141] op_sel_hi:[1,0]
	v_pk_mul_f32 v[122:123], v[116:117], v[140:141] op_sel_hi:[1,0]
	v_pk_mul_f32 v[116:117], v[114:115], v[140:141] op_sel_hi:[1,0]
	v_cvt_pk_bf16_f32 v114, v118, v119
	v_cvt_pk_bf16_f32 v115, v120, v121
	v_cvt_pk_bf16_f32 v116, v116, v117
	v_cvt_pk_bf16_f32 v117, v122, v123
	flat_store_dwordx4 v[126:127], v[114:117] offset:256
	ds_read_b32 v114, v139 offset:128
	s_and_b64 vcc, exec, s[10:11]
	v_add_u32_e32 v116, 16, v134
	v_ashrrev_i32_e32 v117, 31, v116
	v_lshlrev_b64 v[116:117], 10, v[116:117]
	v_lshl_add_u64 v[116:117], s[36:37], 0, v[116:117]
	s_waitcnt lgkmcnt(0)
	v_pk_mul_f32 v[108:109], v[108:109], v[114:115] op_sel_hi:[1,0]
	v_pk_mul_f32 v[106:107], v[106:107], v[114:115] op_sel_hi:[1,0]
	v_pk_mul_f32 v[118:119], v[100:101], v[114:115] op_sel_hi:[1,0]
	v_pk_mul_f32 v[100:101], v[98:99], v[114:115] op_sel_hi:[1,0]
	v_cvt_pk_bf16_f32 v98, v106, v107
	v_cvt_pk_bf16_f32 v99, v108, v109
	v_cvt_pk_bf16_f32 v100, v100, v101
	v_cvt_pk_bf16_f32 v101, v118, v119
	v_lshl_add_u64 v[106:107], v[116:117], 0, v[0:1]
	flat_store_dwordx4 v[106:107], v[98:101]
	v_pk_mul_f32 v[104:105], v[104:105], v[114:115] op_sel_hi:[1,0]
	v_pk_mul_f32 v[102:103], v[102:103], v[114:115] op_sel_hi:[1,0]
	v_pk_mul_f32 v[100:101], v[112:113], v[114:115] op_sel_hi:[1,0]
	v_pk_mul_f32 v[98:99], v[110:111], v[114:115] op_sel_hi:[1,0]
	v_readfirstlane_b32 s10, v0
	v_cvt_pk_bf16_f32 v98, v98, v99
	v_cvt_pk_bf16_f32 v99, v100, v101
	v_cvt_pk_bf16_f32 v100, v102, v103
	v_cvt_pk_bf16_f32 v101, v104, v105
	flat_store_dwordx4 v[106:107], v[98:101] offset:256
	ds_read_b32 v98, v139 offset:256
	v_readlane_b32 s55, v255, 18
	v_add_u32_e32 v100, 32, v134
	v_ashrrev_i32_e32 v101, 31, v100
	v_lshlrev_b64 v[100:101], 10, v[100:101]
	v_lshl_add_u64 v[100:101], s[36:37], 0, v[100:101]
	s_waitcnt lgkmcnt(0)
	v_pk_mul_f32 v[92:93], v[92:93], v[98:99] op_sel_hi:[1,0]
	v_pk_mul_f32 v[90:91], v[90:91], v[98:99] op_sel_hi:[1,0]
	v_pk_mul_f32 v[102:103], v[84:85], v[98:99] op_sel_hi:[1,0]
	v_pk_mul_f32 v[84:85], v[82:83], v[98:99] op_sel_hi:[1,0]
	v_cvt_pk_bf16_f32 v82, v90, v91
	v_cvt_pk_bf16_f32 v83, v92, v93
	v_cvt_pk_bf16_f32 v84, v84, v85
	v_cvt_pk_bf16_f32 v85, v102, v103
	v_lshl_add_u64 v[90:91], v[100:101], 0, v[0:1]
	flat_store_dwordx4 v[90:91], v[82:85]
	v_pk_mul_f32 v[88:89], v[88:89], v[98:99] op_sel_hi:[1,0]
	v_pk_mul_f32 v[86:87], v[86:87], v[98:99] op_sel_hi:[1,0]
	v_pk_mul_f32 v[84:85], v[96:97], v[98:99] op_sel_hi:[1,0]
	v_pk_mul_f32 v[82:83], v[94:95], v[98:99] op_sel_hi:[1,0]
	v_mov_b32_e32 v236, 0x358637bd
	v_cvt_pk_bf16_f32 v82, v82, v83
	v_cvt_pk_bf16_f32 v83, v84, v85
	v_cvt_pk_bf16_f32 v84, v86, v87
	v_cvt_pk_bf16_f32 v85, v88, v89
	flat_store_dwordx4 v[90:91], v[82:85] offset:256
	ds_read_b32 v82, v139 offset:384
	v_mov_b32_e32 v235, v252
	v_add_u32_e32 v84, 48, v134
	v_ashrrev_i32_e32 v85, 31, v84
	v_lshlrev_b64 v[84:85], 10, v[84:85]
	v_lshl_add_u64 v[84:85], s[36:37], 0, v[84:85]
	s_waitcnt lgkmcnt(0)
	v_pk_mul_f32 v[60:61], v[60:61], v[82:83] op_sel_hi:[1,0]
	v_pk_mul_f32 v[58:59], v[58:59], v[82:83] op_sel_hi:[1,0]
	v_pk_mul_f32 v[86:87], v[52:53], v[82:83] op_sel_hi:[1,0]
	v_pk_mul_f32 v[52:53], v[50:51], v[82:83] op_sel_hi:[1,0]
	v_cvt_pk_bf16_f32 v50, v58, v59
	v_cvt_pk_bf16_f32 v51, v60, v61
	v_cvt_pk_bf16_f32 v52, v52, v53
	v_cvt_pk_bf16_f32 v53, v86, v87
	v_lshl_add_u64 v[58:59], v[84:85], 0, v[0:1]
	flat_store_dwordx4 v[58:59], v[50:53]
	v_pk_mul_f32 v[56:57], v[56:57], v[82:83] op_sel_hi:[1,0]
	v_pk_mul_f32 v[54:55], v[54:55], v[82:83] op_sel_hi:[1,0]
	v_pk_mul_f32 v[52:53], v[64:65], v[82:83] op_sel_hi:[1,0]
	v_pk_mul_f32 v[50:51], v[62:63], v[82:83] op_sel_hi:[1,0]
	v_mov_b64_e32 v[248:249], 0x480
	v_cvt_pk_bf16_f32 v50, v50, v51
	v_cvt_pk_bf16_f32 v51, v52, v53
	v_cvt_pk_bf16_f32 v52, v54, v55
	v_cvt_pk_bf16_f32 v53, v56, v57
	flat_store_dwordx4 v[58:59], v[50:53] offset:256
	ds_read_b32 v54, v139 offset:1024
	v_mov_b64_e32 v[238:239], 0x47f
	v_add_u32_e32 v50, 0x80, v134
	v_ashrrev_i32_e32 v51, 31, v50
	v_lshlrev_b64 v[50:51], 10, v[50:51]
	v_lshl_add_u64 v[56:57], s[36:37], 0, v[50:51]
	s_waitcnt lgkmcnt(0)
; #define LAS __attribute__((address_space(3)))
; __device__ __forceinline__ u32x4 pack8(f32x4 a, f32x4 b) { u32x4 w; w.x = pk2(a[0], a[1]); w.y = pk2(a[2], a[3]); w.z = pk2(b[0], b[1]); w.w = pk2(b[2], b[3]); return w; }
; __device__ __forceinline__ float rstd_part4(const float* p, float inv_n) { const f32x4 a = ((const f32x4*)p)[0]; return 1.0f / sqrtf(((a[0] + a[1]) + (a[2] + a[3])) * inv_n + EPS); }
; __device__ __forceinline__ f32x2 rtab_get(LAS unsigned char* lds, int ui, int r) { return ((const LAS f32x2*)(lds + RTAB_OFF))[(ui & 1) * 256 + r]; }
;     EPI_NOMID
;     __device__ __forceinline__ void begin(const Unit& u, int ui, int tid, LAS unsigned char* lds) const { if (tid < 256) rtab_put(lds, ui, tid, rstd_part4(RS + (size_t)(u.pm * 256 + tid) * 4, 1.f / KVRANK), 0.f); }
;     __device__ __forceinline__ void operator()(const f32x4 (&acc)[2][2][4][2], const Unit& u, int ui, int wr, int wc, int fr, int fq, LAS unsigned char* lds) const {
;         bf16_t* dst = u.pn < 2 ? KN : VM; const int cb = (u.pn & 1) * 256;
; #pragma unroll
;         for (int ai = 0; ai < 2; ++ai)
; #pragma unroll
;             for (int m = 0; m < 4; ++m) {
;                 const int rr = ai * 128 + wr * 64 + m * 16 + fr, row = u.pm * 256 + rr; const float rs = rtab_get(lds, ui, rr)[0];
; #pragma unroll
;                 for (int bj = 0; bj < 2; ++bj) { const int c = cb + bj * 128 + wc * 32 + fq * 8;
;                     *(u32x4*)(dst + (size_t)row * 512 + c) = pack8(acc[ai][bj][m][0] * rs, acc[ai][bj][m][1] * rs); }
;             }
	v_pk_mul_f32 v[52:53], v[76:77], v[54:55] op_sel_hi:[1,0]
	v_pk_mul_f32 v[50:51], v[74:75], v[54:55] op_sel_hi:[1,0]
	v_pk_mul_f32 v[58:59], v[68:69], v[54:55] op_sel_hi:[1,0]
	v_pk_mul_f32 v[60:61], v[66:67], v[54:55] op_sel_hi:[1,0]
	v_cvt_pk_bf16_f32 v50, v50, v51
	v_cvt_pk_bf16_f32 v51, v52, v53
	v_cvt_pk_bf16_f32 v52, v60, v61
	v_cvt_pk_bf16_f32 v53, v58, v59
	v_lshl_add_u64 v[56:57], v[56:57], 0, v[0:1]
	flat_store_dwordx4 v[56:57], v[50:53]
	v_pk_mul_f32 v[58:59], v[72:73], v[54:55] op_sel_hi:[1,0]
	v_mov_b32_e32 v234, 0x30000
	v_pk_mul_f32 v[52:53], v[80:81], v[54:55] op_sel_hi:[1,0]
	v_pk_mul_f32 v[50:51], v[78:79], v[54:55] op_sel_hi:[1,0]
	v_pk_mul_f32 v[54:55], v[70:71], v[54:55] op_sel_hi:[1,0]
	v_cvt_pk_bf16_f32 v50, v50, v51
	v_cvt_pk_bf16_f32 v51, v52, v53
	v_cvt_pk_bf16_f32 v52, v54, v55
	v_cvt_pk_bf16_f32 v53, v58, v59
	flat_store_dwordx4 v[56:57], v[50:53] offset:256
	ds_read_b32 v50, v139 offset:1152
	s_waitcnt lgkmcnt(0)
	v_pk_mul_f32 v[44:45], v[44:45], v[50:51] op_sel_hi:[1,0]
	v_add_u32_e32 v52, 0x90, v134
	v_ashrrev_i32_e32 v53, 31, v52
	v_lshlrev_b64 v[52:53], 10, v[52:53]
	v_lshl_add_u64 v[52:53], s[36:37], 0, v[52:53]
	v_pk_mul_f32 v[42:43], v[42:43], v[50:51] op_sel_hi:[1,0]
	v_pk_mul_f32 v[54:55], v[36:37], v[50:51] op_sel_hi:[1,0]
	v_pk_mul_f32 v[36:37], v[34:35], v[50:51] op_sel_hi:[1,0]
	v_cvt_pk_bf16_f32 v34, v42, v43
	v_cvt_pk_bf16_f32 v35, v44, v45
	v_cvt_pk_bf16_f32 v36, v36, v37
	v_cvt_pk_bf16_f32 v37, v54, v55
	v_lshl_add_u64 v[42:43], v[52:53], 0, v[0:1]
	flat_store_dwordx4 v[42:43], v[34:37]
	v_pk_mul_f32 v[40:41], v[40:41], v[50:51] op_sel_hi:[1,0]
	v_pk_mul_f32 v[38:39], v[38:39], v[50:51] op_sel_hi:[1,0]
	v_pk_mul_f32 v[36:37], v[48:49], v[50:51] op_sel_hi:[1,0]
	v_pk_mul_f32 v[34:35], v[46:47], v[50:51] op_sel_hi:[1,0]
	s_nop 0
	v_cvt_pk_bf16_f32 v34, v34, v35
	v_cvt_pk_bf16_f32 v35, v36, v37
	v_cvt_pk_bf16_f32 v36, v38, v39
	v_cvt_pk_bf16_f32 v37, v40, v41
	flat_store_dwordx4 v[42:43], v[34:37] offset:256
	ds_read_b32 v34, v139 offset:1280
	s_waitcnt lgkmcnt(0)
	v_pk_mul_f32 v[28:29], v[28:29], v[34:35] op_sel_hi:[1,0]
	v_add_u32_e32 v36, 0xa0, v134
	v_ashrrev_i32_e32 v37, 31, v36
	v_lshlrev_b64 v[36:37], 10, v[36:37]
	v_lshl_add_u64 v[36:37], s[36:37], 0, v[36:37]
	v_pk_mul_f32 v[26:27], v[26:27], v[34:35] op_sel_hi:[1,0]
	v_pk_mul_f32 v[38:39], v[20:21], v[34:35] op_sel_hi:[1,0]
	v_pk_mul_f32 v[20:21], v[18:19], v[34:35] op_sel_hi:[1,0]
	v_cvt_pk_bf16_f32 v18, v26, v27
	v_cvt_pk_bf16_f32 v19, v28, v29
	v_cvt_pk_bf16_f32 v20, v20, v21
	v_cvt_pk_bf16_f32 v21, v38, v39
	v_lshl_add_u64 v[26:27], v[36:37], 0, v[0:1]
	flat_store_dwordx4 v[26:27], v[18:21]
	v_pk_mul_f32 v[24:25], v[24:25], v[34:35] op_sel_hi:[1,0]
	v_pk_mul_f32 v[22:23], v[22:23], v[34:35] op_sel_hi:[1,0]
	v_pk_mul_f32 v[20:21], v[32:33], v[34:35] op_sel_hi:[1,0]
	v_pk_mul_f32 v[18:19], v[30:31], v[34:35] op_sel_hi:[1,0]
	s_nop 0
	v_cvt_pk_bf16_f32 v18, v18, v19
	v_cvt_pk_bf16_f32 v19, v20, v21
	v_cvt_pk_bf16_f32 v20, v22, v23
	v_cvt_pk_bf16_f32 v21, v24, v25
	flat_store_dwordx4 v[26:27], v[18:21] offset:256
	ds_read_b32 v18, v139 offset:1408
	s_waitcnt lgkmcnt(0)
	v_pk_mul_f32 v[12:13], v[12:13], v[18:19] op_sel_hi:[1,0]
	v_add_u32_e32 v20, 0xb0, v134
	v_ashrrev_i32_e32 v21, 31, v20
	v_lshlrev_b64 v[20:21], 10, v[20:21]
	v_lshl_add_u64 v[20:21], s[36:37], 0, v[20:21]
	v_pk_mul_f32 v[10:11], v[10:11], v[18:19] op_sel_hi:[1,0]
	v_pk_mul_f32 v[22:23], v[4:5], v[18:19] op_sel_hi:[1,0]
	v_pk_mul_f32 v[4:5], v[2:3], v[18:19] op_sel_hi:[1,0]
	v_cvt_pk_bf16_f32 v2, v10, v11
	v_cvt_pk_bf16_f32 v3, v12, v13
	v_cvt_pk_bf16_f32 v4, v4, v5
	v_cvt_pk_bf16_f32 v5, v22, v23
	v_lshl_add_u64 v[10:11], v[20:21], 0, v[0:1]
	flat_store_dwordx4 v[10:11], v[2:5]
	v_pk_mul_f32 v[8:9], v[8:9], v[18:19] op_sel_hi:[1,0]
	v_pk_mul_f32 v[6:7], v[6:7], v[18:19] op_sel_hi:[1,0]
	v_pk_mul_f32 v[4:5], v[16:17], v[18:19] op_sel_hi:[1,0]
	v_pk_mul_f32 v[2:3], v[14:15], v[18:19] op_sel_hi:[1,0]
	v_mov_b32_e32 v0, 0x260
	v_cvt_pk_bf16_f32 v2, v2, v3
	v_cvt_pk_bf16_f32 v3, v4, v5
	v_cvt_pk_bf16_f32 v4, v6, v7
	v_cvt_pk_bf16_f32 v5, v8, v9
	s_mov_b64 s[36:37], -1
	v_mov_b32_e32 v251, v0
	flat_store_dwordx4 v[10:11], v[2:5] offset:256
	s_cbranch_vccnz .LBB0_702
	s_and_saveexec_b64 s[36:37], s[8:9]
	s_cbranch_execz .LBB0_716
	s_mov_b32 s10, 0xf800000
	s_waitcnt vmcnt(0) lgkmcnt(0)
	v_mov_b32_e32 v2, v240
	v_mov_b32_e32 v3, v241
	v_mov_b32_e32 v4, v242
	v_mov_b32_e32 v5, v243
	v_mov_b32_e32 v6, v3
	v_mov_b32_e32 v7, v4
	v_mov_b32_e32 v3, v5
	v_pk_add_f32 v[2:3], v[6:7], v[2:3]
	s_nop 0
	v_add_f32_e32 v0, v2, v3
	v_fmamk_f32 v0, v0, 0x3b800000, v236
	v_cmp_gt_f32_e32 vcc, s10, v0
	v_mul_f32_e32 v2, 0x4f800000, v0
	s_nop 0
	v_cndmask_b32_e32 v0, v0, v2, vcc
	v_sqrt_f32_e32 v2, v0
	s_nop 0
	v_add_u32_e32 v3, -1, v2
	v_fma_f32 v4, -v3, v2, v0
	v_cmp_ge_f32_e64 s[10:11], 0, v4
	v_add_u32_e32 v4, 1, v2
	s_nop 0
	v_cndmask_b32_e64 v3, v2, v3, s[10:11]
	v_fma_f32 v2, -v4, v2, v0
	v_cmp_lt_f32_e64 s[10:11], 0, v2
	s_nop 1
	v_cndmask_b32_e64 v2, v3, v4, s[10:11]
	v_mul_f32_e32 v3, 0x37800000, v2
	v_cndmask_b32_e32 v2, v2, v3, vcc
	v_cmp_class_f32_e32 vcc, v0, v251
	s_nop 1
	v_cndmask_b32_e32 v0, v2, v0, vcc
	v_div_scale_f32 v2, s[10:11], v0, v0, 1.0
	v_rcp_f32_e32 v3, v2
	s_add_i32 s10, s44, 0x100
	s_and_b32 s10, s10, 0x100
	s_lshl_b32 s10, s10, 3
	v_fma_f32 v4, -v2, v3, 1.0
	v_fmac_f32_e32 v3, v4, v3
	v_div_scale_f32 v4, vcc, 1.0, v0, 1.0
	v_mul_f32_e32 v5, v4, v3
	v_fma_f32 v6, -v2, v5, v4
	v_fmac_f32_e32 v5, v6, v3
	v_fma_f32 v2, -v2, v5, v4
	v_div_fmas_f32 v2, v2, v3, v5
	v_div_fixup_f32 v0, v2, v0, 1.0
	v_mov_b32_e32 v2, v188
	s_add_i32 s10, s10, 0
	v_lshl_add_u32 v2, v2, 3, s10
	v_add_u32_e32 v2, 0x22400, v2
	ds_write_b64 v2, v[0:1]
